# speedup vs baseline: 1.0582x; 1.0159x over previous
.LBB0_3:
	s_cmpk_lt_u32 s2, 0x300
	s_cbranch_scc0 .Lprep_nodelay
	s_sleep 40
